# baseline (speedup 1.0000x reference)
_Z9k_binsortPKjPKiPKfPKDv4_jPiS8_PfP6__half:
	s_load_dwordx4 s[80:83], s[0:1], 0x0
	s_load_dwordx8 s[72:79], s[0:1], 0x18
	s_cmpk_ge_u32 s2, 0x200
	s_cbranch_scc1 .Lk2_prio
	s_setprio 1
	s_cmpk_ge_u32 s2, 0x100
	s_cbranch_scc1 .Lk2_prio
	s_setprio 2
.Lk2_prio:
	v_lshl_or_b32 v2, s2, 8, v0
	v_ashrrev_i32_e32 v3, 31, v2
	v_lshlrev_b32_e32 v70, 4, v0
	s_waitcnt lgkmcnt(0)
	v_lshl_add_u64 v[10:11], v[2:3], 2, s[82:83]
	global_load_dwordx4 v[6:9], v70, s[72:73]
	global_load_dword v3, v[10:11], off
	global_load_dword v4, v[10:11], off offset:1024
	s_movk_i32 s3, 0x241
	v_cmp_gt_u32_e32 vcc, s3, v0
	s_waitcnt vmcnt(2)
	ds_write_b128 v70, v[6:9] offset:24576
	s_and_saveexec_b64 s[6:7], vcc
	s_cbranch_execz .LBB1_7
	v_sub_u32_e32 v1, 0x240, v0
	v_lshrrev_b32_e32 v2, 8, v1
	v_add_u32_e32 v1, 2, v2
	v_mov_b32_e32 v6, 0x7000
	s_mov_b32 s8, 0
	v_and_b32_e32 v5, 6, v1
	v_mov_b32_e32 v1, v2
	v_lshl_or_b32 v6, v0, 2, v6
	s_mov_b32 s9, 1
	s_mov_b64 s[10:11], 0
	v_mov_b32_e32 v7, 0
	s_mov_b32 s12, s8
	s_branch .LBB1_3
